# near-tie rescoring before END barrier, v2: epilogue gathers first, fixed 12-load tie fetch, then stores
# baseline (speedup 1.0000x reference)
.LBB1_65:
	s_lshl_b32 s88, s33, 5
	s_add_i32 s88, s88, s98
	s_add_i32 s88, s88, 0x18004
	s_lshl_b32 s88, s88, 10
	s_add_u32 s88, s14, s88
	s_addc_u32 s89, s15, 0
	s_add_u32 s90, s88, 0x2000
	s_addc_u32 s91, s89, 0
	s_add_u32 s92, s90, 0x2000
	s_addc_u32 s93, s91, 0
	s_add_u32 s94, s92, 0x2000
	s_addc_u32 s95, s93, 0
	v_readlane_b32 s52, v14, 0
	v_readlane_b32 s53, v14, 1
	v_readlane_b32 s54, v14, 2
	v_readlane_b32 s55, v14, 3
	v_readlane_b32 s56, v14, 4
	v_readlane_b32 s57, v14, 5
	v_readlane_b32 s58, v14, 6
	v_readlane_b32 s59, v14, 7
	v_readlane_b32 s68, v14, 8
	v_readlane_b32 s69, v14, 9
	v_readlane_b32 s70, v14, 10
	v_readlane_b32 s71, v14, 11
	v_readlane_b32 s72, v14, 12
	v_readlane_b32 s73, v14, 13
	v_readlane_b32 s74, v14, 14
	v_readlane_b32 s75, v14, 15
	v_readlane_b32 s76, v14, 16
	v_readlane_b32 s77, v14, 17
	v_readlane_b32 s78, v14, 18
	v_readlane_b32 s79, v14, 19
	v_readlane_b32 s80, v14, 20
	v_readlane_b32 s81, v14, 21
	v_readlane_b32 s82, v14, 22
	v_readlane_b32 s83, v14, 23
	v_readlane_b32 s84, v14, 24
	v_readlane_b32 s85, v14, 25
	v_readlane_b32 s86, v14, 26
	v_readlane_b32 s87, v14, 27
	v_readlane_b32 s98, v14, 28
	v_readlane_b32 s99, v14, 29
	v_readlane_b32 s100, v14, 30
	v_readlane_b32 s101, v14, 31
	v_lshl_or_b32 v192, s52, 10, v162
	v_lshl_or_b32 v193, s53, 10, v162
	v_lshl_or_b32 v194, s54, 10, v162
	v_lshl_or_b32 v195, s55, 10, v162
	v_lshl_or_b32 v196, s56, 10, v162
	v_lshl_or_b32 v197, s57, 10, v162
	v_lshl_or_b32 v198, s58, 10, v162
	v_lshl_or_b32 v199, s59, 10, v162
	global_load_dwordx4 v[50:53], v192, s[18:19]
	global_load_dwordx4 v[54:57], v193, s[18:19]
	global_load_dwordx4 v[58:61], v194, s[18:19]
	global_load_dwordx4 v[62:65], v195, s[18:19]
	global_load_dwordx4 v[66:69], v196, s[18:19]
	global_load_dwordx4 v[70:73], v197, s[18:19]
	global_load_dwordx4 v[74:77], v198, s[18:19]
	global_load_dwordx4 v[78:81], v199, s[18:19]
	v_lshl_or_b32 v192, s68, 10, v162
	v_lshl_or_b32 v193, s69, 10, v162
	v_lshl_or_b32 v194, s70, 10, v162
	v_lshl_or_b32 v195, s71, 10, v162
	v_lshl_or_b32 v196, s72, 10, v162
	v_lshl_or_b32 v197, s73, 10, v162
	v_lshl_or_b32 v198, s74, 10, v162
	v_lshl_or_b32 v199, s75, 10, v162
	global_load_dwordx4 v[82:85], v192, s[18:19]
	global_load_dwordx4 v[86:89], v193, s[18:19]
	global_load_dwordx4 v[90:93], v194, s[18:19]
	global_load_dwordx4 v[94:97], v195, s[18:19]
	global_load_dwordx4 v[98:101], v196, s[18:19]
	global_load_dwordx4 v[102:105], v197, s[18:19]
	global_load_dwordx4 v[106:109], v198, s[18:19]
	global_load_dwordx4 v[110:113], v199, s[18:19]
	v_lshl_or_b32 v192, s76, 10, v162
	v_lshl_or_b32 v193, s77, 10, v162
	v_lshl_or_b32 v194, s78, 10, v162
	v_lshl_or_b32 v195, s79, 10, v162
	v_lshl_or_b32 v196, s80, 10, v162
	v_lshl_or_b32 v197, s81, 10, v162
	v_lshl_or_b32 v198, s82, 10, v162
	v_lshl_or_b32 v199, s83, 10, v162
	global_load_dwordx4 v[114:117], v192, s[18:19]
	global_load_dwordx4 v[118:121], v193, s[18:19]
	global_load_dwordx4 v[122:125], v194, s[18:19]
	global_load_dwordx4 v[126:129], v195, s[18:19]
	global_load_dwordx4 v[130:133], v196, s[18:19]
	global_load_dwordx4 v[134:137], v197, s[18:19]
	global_load_dwordx4 v[138:141], v198, s[18:19]
	global_load_dwordx4 v[142:145], v199, s[18:19]
	v_lshl_or_b32 v192, s84, 10, v162
	v_lshl_or_b32 v193, s85, 10, v162
	v_lshl_or_b32 v194, s86, 10, v162
	v_lshl_or_b32 v195, s87, 10, v162
	v_lshl_or_b32 v196, s98, 10, v162
	v_lshl_or_b32 v197, s99, 10, v162
	v_lshl_or_b32 v198, s100, 10, v162
	v_lshl_or_b32 v199, s101, 10, v162
	global_load_dwordx4 v[146:149], v192, s[18:19]
	global_load_dwordx4 v[150:153], v193, s[18:19]
	global_load_dwordx4 v[154:157], v194, s[18:19]
	global_load_dwordx4 v[158:161], v195, s[18:19]
	global_load_dwordx4 v[176:179], v196, s[18:19]
	global_load_dwordx4 v[180:183], v197, s[18:19]
	global_load_dwordx4 v[184:187], v198, s[18:19]
	global_load_dwordx4 v[188:191], v199, s[18:19]
	s_mov_b64 exec, -1
	v_mbcnt_lo_u32_b32 v200, -1, 0
	v_mbcnt_hi_u32_b32 v200, -1, v200
	v_lshlrev_b32_e32 v201, 4, v200
	v_xor_b32_e32 v202, 32, v200
	v_lshlrev_b32_e32 v202, 2, v202
	v_xor_b32_e32 v203, 16, v200
	v_lshlrev_b32_e32 v203, 2, v203
	v_xor_b32_e32 v204, 8, v200
	v_lshlrev_b32_e32 v204, 2, v204
	v_xor_b32_e32 v205, 4, v200
	v_lshlrev_b32_e32 v205, 2, v205
	v_xor_b32_e32 v206, 2, v200
	v_lshlrev_b32_e32 v206, 2, v206
	v_xor_b32_e32 v207, 1, v200
	v_lshlrev_b32_e32 v207, 2, v207
	v_mov_b32_e32 v208, 0x22630
	ds_read_b32 v208, v208
	s_mov_b32 s51, s33
	s_waitcnt lgkmcnt(0)
	v_readfirstlane_b32 s50, v208
	s_nop 3
	s_mov_b32 s48, 0
	s_add_i32 s49, s51, 0
	s_cmp_lt_i32 s49, s50
	s_cbranch_scc0 .Lpt_dm_c_0
	s_lshl_b32 s60, s49, 2
	s_add_i32 s61, s60, 0x21800
	s_add_i32 s60, s60, 0x21000
	v_mov_b32_e32 v208, s61
	v_mov_b32_e32 v209, s60
	ds_read_b32 v208, v208
	ds_read_b32 v209, v209
	s_waitcnt lgkmcnt(0)
	v_readfirstlane_b32 s40, v208
	v_readfirstlane_b32 s44, v209
	s_nop 3
	s_lshl_b32 s62, s40, 10
	s_add_u32 s62, s16, s62
	s_addc_u32 s63, s17, 0
	global_load_dwordx4 v[2:5], v201, s[62:63]
	s_and_b32 s64, s44, 0x1ff
	s_bfe_u32 s65, s44, 0x90009
	s_bfe_u32 s66, s44, 0x90012
	v_lshl_or_b32 v210, s64, 10, v201
	v_lshl_or_b32 v211, s65, 10, v201
	v_lshl_or_b32 v212, s66, 10, v201
	global_load_dwordx4 v[6:9], v210, s[18:19]
	global_load_dwordx4 v[10:13], v211, s[18:19]
	global_load_dwordx4 v[14:17], v212, s[18:19]
	s_mov_b32 s48, 1
	s_branch .Lpt_dn_c_0
.Lpt_dm_c_0:
	global_load_dwordx4 v[2:5], v201, s[18:19]
	global_load_dwordx4 v[6:9], v201, s[18:19]
	global_load_dwordx4 v[10:13], v201, s[18:19]
	global_load_dwordx4 v[14:17], v201, s[18:19]
.Lpt_dn_c_0:
	s_add_i32 s49, s51, 8
	s_cmp_lt_i32 s49, s50
	s_cbranch_scc0 .Lpt_dm_c_1
	s_lshl_b32 s60, s49, 2
	s_add_i32 s61, s60, 0x21800
	s_add_i32 s60, s60, 0x21000
	v_mov_b32_e32 v208, s61
	v_mov_b32_e32 v209, s60
	ds_read_b32 v208, v208
	ds_read_b32 v209, v209
	s_waitcnt lgkmcnt(0)
	v_readfirstlane_b32 s41, v208
	v_readfirstlane_b32 s45, v209
	s_nop 3
	s_lshl_b32 s62, s41, 10
	s_add_u32 s62, s16, s62
	s_addc_u32 s63, s17, 0
	global_load_dwordx4 v[18:21], v201, s[62:63]
	s_and_b32 s64, s45, 0x1ff
	s_bfe_u32 s65, s45, 0x90009
	s_bfe_u32 s66, s45, 0x90012
	v_lshl_or_b32 v210, s64, 10, v201
	v_lshl_or_b32 v211, s65, 10, v201
	v_lshl_or_b32 v212, s66, 10, v201
	global_load_dwordx4 v[22:25], v210, s[18:19]
	global_load_dwordx4 v[26:29], v211, s[18:19]
	global_load_dwordx4 v[30:33], v212, s[18:19]
	s_mov_b32 s48, 2
	s_branch .Lpt_dn_c_1
.Lpt_dm_c_1:
	global_load_dwordx4 v[18:21], v201, s[18:19]
	global_load_dwordx4 v[22:25], v201, s[18:19]
	global_load_dwordx4 v[26:29], v201, s[18:19]
	global_load_dwordx4 v[30:33], v201, s[18:19]
.Lpt_dn_c_1:
	s_add_i32 s49, s51, 16
	s_cmp_lt_i32 s49, s50
	s_cbranch_scc0 .Lpt_dm_c_2
	s_lshl_b32 s60, s49, 2
	s_add_i32 s61, s60, 0x21800
	s_add_i32 s60, s60, 0x21000
	v_mov_b32_e32 v208, s61
	v_mov_b32_e32 v209, s60
	ds_read_b32 v208, v208
	ds_read_b32 v209, v209
	s_waitcnt lgkmcnt(0)
	v_readfirstlane_b32 s42, v208
	v_readfirstlane_b32 s46, v209
	s_nop 3
	s_lshl_b32 s62, s42, 10
	s_add_u32 s62, s16, s62
	s_addc_u32 s63, s17, 0
	global_load_dwordx4 v[34:37], v201, s[62:63]
	s_and_b32 s64, s46, 0x1ff
	s_bfe_u32 s65, s46, 0x90009
	s_bfe_u32 s66, s46, 0x90012
	v_lshl_or_b32 v210, s64, 10, v201
	v_lshl_or_b32 v211, s65, 10, v201
	v_lshl_or_b32 v212, s66, 10, v201
	global_load_dwordx4 v[38:41], v210, s[18:19]
	global_load_dwordx4 v[42:45], v211, s[18:19]
	global_load_dwordx4 v[46:49], v212, s[18:19]
	s_mov_b32 s48, 3
	s_branch .Lpt_dn_c_2
.Lpt_dm_c_2:
	global_load_dwordx4 v[34:37], v201, s[18:19]
	global_load_dwordx4 v[38:41], v201, s[18:19]
	global_load_dwordx4 v[42:45], v201, s[18:19]
	global_load_dwordx4 v[46:49], v201, s[18:19]
.Lpt_dn_c_2:
	s_waitcnt vmcnt(43)
	global_store_dwordx4 v162, v[50:53], s[88:89] offset:-4096 nt
	s_waitcnt vmcnt(43)
	global_store_dwordx4 v162, v[54:57], s[88:89] offset:-3072 nt
	s_waitcnt vmcnt(43)
	global_store_dwordx4 v162, v[58:61], s[88:89] offset:-2048 nt
	s_waitcnt vmcnt(43)
	global_store_dwordx4 v162, v[62:65], s[88:89] offset:-1024 nt
	s_waitcnt vmcnt(43)
	global_store_dwordx4 v162, v[66:69], s[88:89] offset:0 nt
	s_waitcnt vmcnt(43)
	global_store_dwordx4 v162, v[70:73], s[88:89] offset:1024 nt
	s_waitcnt vmcnt(43)
	global_store_dwordx4 v162, v[74:77], s[88:89] offset:2048 nt
	s_waitcnt vmcnt(43)
	global_store_dwordx4 v162, v[78:81], s[88:89] offset:3072 nt
	s_waitcnt vmcnt(43)
	global_store_dwordx4 v162, v[82:85], s[90:91] offset:-4096 nt
	s_waitcnt vmcnt(43)
	global_store_dwordx4 v162, v[86:89], s[90:91] offset:-3072 nt
	s_waitcnt vmcnt(43)
	global_store_dwordx4 v162, v[90:93], s[90:91] offset:-2048 nt
	s_waitcnt vmcnt(43)
	global_store_dwordx4 v162, v[94:97], s[90:91] offset:-1024 nt
	s_waitcnt vmcnt(43)
	global_store_dwordx4 v162, v[98:101], s[90:91] offset:0 nt
	s_waitcnt vmcnt(43)
	global_store_dwordx4 v162, v[102:105], s[90:91] offset:1024 nt
	s_waitcnt vmcnt(43)
	global_store_dwordx4 v162, v[106:109], s[90:91] offset:2048 nt
	s_waitcnt vmcnt(43)
	global_store_dwordx4 v162, v[110:113], s[90:91] offset:3072 nt
	s_waitcnt vmcnt(43)
	global_store_dwordx4 v162, v[114:117], s[92:93] offset:-4096 nt
	s_waitcnt vmcnt(43)
	global_store_dwordx4 v162, v[118:121], s[92:93] offset:-3072 nt
	s_waitcnt vmcnt(43)
	global_store_dwordx4 v162, v[122:125], s[92:93] offset:-2048 nt
	s_waitcnt vmcnt(43)
	global_store_dwordx4 v162, v[126:129], s[92:93] offset:-1024 nt
	s_waitcnt vmcnt(43)
	global_store_dwordx4 v162, v[130:133], s[92:93] offset:0 nt
	s_waitcnt vmcnt(43)
	global_store_dwordx4 v162, v[134:137], s[92:93] offset:1024 nt
	s_waitcnt vmcnt(43)
	global_store_dwordx4 v162, v[138:141], s[92:93] offset:2048 nt
	s_waitcnt vmcnt(43)
	global_store_dwordx4 v162, v[142:145], s[92:93] offset:3072 nt
	s_waitcnt vmcnt(43)
	global_store_dwordx4 v162, v[146:149], s[94:95] offset:-4096 nt
	s_waitcnt vmcnt(43)
	global_store_dwordx4 v162, v[150:153], s[94:95] offset:-3072 nt
	s_waitcnt vmcnt(43)
	global_store_dwordx4 v162, v[154:157], s[94:95] offset:-2048 nt
	s_waitcnt vmcnt(43)
	global_store_dwordx4 v162, v[158:161], s[94:95] offset:-1024 nt
	s_waitcnt vmcnt(43)
	global_store_dwordx4 v162, v[176:179], s[94:95] offset:0 nt
	s_waitcnt vmcnt(43)
	global_store_dwordx4 v162, v[180:183], s[94:95] offset:1024 nt
	s_waitcnt vmcnt(43)
	global_store_dwordx4 v162, v[184:187], s[94:95] offset:2048 nt
	s_waitcnt vmcnt(43)
	global_store_dwordx4 v162, v[188:191], s[94:95] offset:3072 nt
	s_waitcnt vmcnt(32)
	s_branch .Lpt_picks
	s_branch .LBB1_5
